# K2 epilogue: wave reduction by DPP row ops + readlanes instead of six ds_bpermute round trips
# baseline (speedup 1.0000x reference)
.LBB1_6:
	s_and_b32 s6, s26, 1
	v_lshl_add_u32 v143, s6, 14, v142
	s_waitcnt vmcnt(14)
	v_lshl_add_u32 v162, s6, 13, v137
	v_add_u32_e32 v160, v143, v141
	ds_read_b128 v[144:147], v162
	ds_read_b128 v[148:151], v162 offset:1024
	ds_read_b128 v[152:155], v160
	ds_read_b128 v[156:159], v160 offset:4096
	s_waitcnt lgkmcnt(0)
	v_mfma_f32_32x32x16_f16 v[114:129], v[152:155], v[144:147], v[114:129]
	s_and_b32 s6, s13, 0xf0000
	s_and_b32 s27, s15, 0x2000
	v_add_u32_e32 v163, v143, v140
	s_add_i32 s26, s26, 1
	s_addk_i32 s15, 0x2000
	s_add_i32 s13, s13, 0x10000
	v_mfma_f32_32x32x16_f16 v[50:65], v[152:155], v[148:151], v[50:65]
	v_mfma_f32_32x32x16_f16 v[82:97], v[156:159], v[144:147], v[82:97]
	v_mfma_f32_32x32x16_f16 v[18:33], v[156:159], v[148:151], v[18:33]
	ds_read_b128 v[152:155], v160 offset:8192
	ds_read_b128 v[156:159], v160 offset:12288
	v_lshl_add_u64 v[160:161], v[130:131], 0, s[6:7]
	s_add_i32 s6, s3, s27
	s_waitcnt lgkmcnt(0)
	s_mov_b32 m0, s6
	s_nop 0
	global_load_lds_dwordx4 v[160:161], off
	s_waitcnt lgkmcnt(0)
	v_mfma_f32_32x32x16_f16 v[98:113], v[152:155], v[144:147], v[98:113]
	s_add_i32 m0, s6, 0x400
	v_mfma_f32_32x32x16_f16 v[34:49], v[152:155], v[148:151], v[34:49]
	v_lshl_add_u64 v[152:153], v[160:161], 0, s[4:5]
	global_load_lds_dwordx4 v[152:153], off
	s_waitcnt vmcnt(14)
	s_add_i32 m0, s6, 0x800
	v_mfma_f32_32x32x16_f16 v[66:81], v[156:159], v[144:147], v[66:81]
	v_mfma_f32_32x32x16_f16 v[2:17], v[156:159], v[148:151], v[2:17]
	ds_read_b128 v[144:147], v163
	ds_read_b128 v[148:151], v162 offset:2048
	ds_read_b128 v[152:155], v162 offset:3072
	ds_read_b128 v[156:159], v163 offset:4096
	s_waitcnt lgkmcnt(0)
	v_mfma_f32_32x32x16_f16 v[114:129], v[144:147], v[148:151], v[114:129]
	v_mfma_f32_32x32x16_f16 v[50:65], v[144:147], v[152:155], v[50:65]
	v_mfma_f32_32x32x16_f16 v[82:97], v[156:159], v[148:151], v[82:97]
	v_mfma_f32_32x32x16_f16 v[18:33], v[156:159], v[152:155], v[18:33]
	ds_read_b128 v[144:147], v163 offset:8192
	ds_read_b128 v[156:159], v163 offset:12288
	s_waitcnt lgkmcnt(0)
	v_add_u32_e32 v163, v143, v139
	v_add_u32_e32 v143, v143, v136
	s_waitcnt lgkmcnt(0)
	v_mfma_f32_32x32x16_f16 v[98:113], v[144:147], v[148:151], v[98:113]
	v_mfma_f32_32x32x16_f16 v[34:49], v[144:147], v[152:155], v[34:49]
	v_lshl_add_u64 v[144:145], v[160:161], 0, s[8:9]
	v_lshl_add_u64 v[146:147], v[160:161], 0, s[16:17]
	global_load_lds_dwordx4 v[144:145], off
	s_add_i32 m0, s6, 0xc00
	s_nop 0
	global_load_lds_dwordx4 v[146:147], off
	s_waitcnt vmcnt(14)
	v_mfma_f32_32x32x16_f16 v[66:81], v[156:159], v[148:151], v[66:81]
	s_add_i32 m0, s6, 0x1000
	v_mfma_f32_32x32x16_f16 v[2:17], v[156:159], v[152:155], v[2:17]
	ds_read_b128 v[144:147], v163
	ds_read_b128 v[148:151], v162 offset:4096
	ds_read_b128 v[152:155], v162 offset:5120
	ds_read_b128 v[156:159], v163 offset:4096
	s_waitcnt lgkmcnt(0)
	v_mfma_f32_32x32x16_f16 v[114:129], v[144:147], v[148:151], v[114:129]
	v_mfma_f32_32x32x16_f16 v[50:65], v[144:147], v[152:155], v[50:65]
	v_mfma_f32_32x32x16_f16 v[82:97], v[156:159], v[148:151], v[82:97]
	v_mfma_f32_32x32x16_f16 v[18:33], v[156:159], v[152:155], v[18:33]
	ds_read_b128 v[144:147], v163 offset:8192
	ds_read_b128 v[156:159], v163 offset:12288
	s_waitcnt lgkmcnt(0)
	s_waitcnt lgkmcnt(0)
	v_mfma_f32_32x32x16_f16 v[98:113], v[144:147], v[148:151], v[98:113]
	v_mfma_f32_32x32x16_f16 v[34:49], v[144:147], v[152:155], v[34:49]
	v_lshl_add_u64 v[144:145], v[160:161], 0, s[18:19]
	v_lshl_add_u64 v[146:147], v[160:161], 0, s[20:21]
	global_load_lds_dwordx4 v[144:145], off
	s_add_i32 m0, s6, 0x1400
	s_nop 0
	global_load_lds_dwordx4 v[146:147], off
	s_waitcnt vmcnt(14)
	v_mfma_f32_32x32x16_f16 v[66:81], v[156:159], v[148:151], v[66:81]
	s_add_i32 m0, s6, 0x1800
	v_mfma_f32_32x32x16_f16 v[2:17], v[156:159], v[152:155], v[2:17]
	ds_read_b128 v[144:147], v143
	ds_read_b128 v[148:151], v162 offset:6144
	ds_read_b128 v[152:155], v162 offset:7168
	ds_read_b128 v[156:159], v143 offset:4096
	s_waitcnt lgkmcnt(0)
	v_mfma_f32_32x32x16_f16 v[114:129], v[144:147], v[148:151], v[114:129]
	v_mfma_f32_32x32x16_f16 v[50:65], v[144:147], v[152:155], v[50:65]
	v_mfma_f32_32x32x16_f16 v[82:97], v[156:159], v[148:151], v[82:97]
	v_mfma_f32_32x32x16_f16 v[18:33], v[156:159], v[152:155], v[18:33]
	ds_read_b128 v[144:147], v143 offset:8192
	ds_read_b128 v[156:159], v143 offset:12288
	s_waitcnt lgkmcnt(0)
	s_waitcnt lgkmcnt(0)
	v_mfma_f32_32x32x16_f16 v[98:113], v[144:147], v[148:151], v[98:113]
	v_mfma_f32_32x32x16_f16 v[34:49], v[144:147], v[152:155], v[34:49]
	v_lshl_add_u64 v[144:145], v[160:161], 0, s[22:23]
	v_lshl_add_u64 v[146:147], v[160:161], 0, s[24:25]
	global_load_lds_dwordx4 v[144:145], off
	s_add_i32 m0, s6, 0x1c00
	s_cmp_eq_u32 s26, 14
	global_load_lds_dwordx4 v[146:147], off
	v_mfma_f32_32x32x16_f16 v[66:81], v[156:159], v[148:151], v[66:81]
	s_waitcnt lgkmcnt(0)
	s_barrier
	v_mfma_f32_32x32x16_f16 v[2:17], v[156:159], v[152:155], v[2:17]
	s_cbranch_scc0 .LBB1_6
	s_waitcnt vmcnt(14)
	v_add_u32_e32 v130, v142, v141
	ds_read_b128 v[144:147], v137
	ds_read_b128 v[148:151], v137 offset:1024
	ds_read_b128 v[152:155], v130
	ds_read_b128 v[156:159], v130 offset:4096
	s_mov_b32 s5, 0
	s_waitcnt lgkmcnt(0)
	v_mfma_f32_32x32x16_f16 v[114:129], v[152:155], v[144:147], v[114:129]
	v_mfma_f32_32x32x16_f16 v[50:65], v[152:155], v[148:151], v[50:65]
	v_mfma_f32_32x32x16_f16 v[82:97], v[156:159], v[144:147], v[82:97]
	v_mfma_f32_32x32x16_f16 v[18:33], v[156:159], v[148:151], v[18:33]
	ds_read_b128 v[152:155], v130 offset:8192
	ds_read_b128 v[156:159], v130 offset:12288
	s_waitcnt vmcnt(12)
	v_add_u32_e32 v130, v142, v140
	s_waitcnt lgkmcnt(0)
	v_mfma_f32_32x32x16_f16 v[98:113], v[152:155], v[144:147], v[98:113]
	v_mfma_f32_32x32x16_f16 v[34:49], v[152:155], v[148:151], v[34:49]
	v_mfma_f32_32x32x16_f16 v[66:81], v[156:159], v[144:147], v[66:81]
	v_mfma_f32_32x32x16_f16 v[2:17], v[156:159], v[148:151], v[2:17]
	ds_read_b128 v[144:147], v137 offset:2048
	ds_read_b128 v[148:151], v137 offset:3072
	ds_read_b128 v[152:155], v130
	ds_read_b128 v[156:159], v130 offset:4096
	s_waitcnt lgkmcnt(0)
	v_mfma_f32_32x32x16_f16 v[114:129], v[152:155], v[144:147], v[114:129]
	v_mfma_f32_32x32x16_f16 v[50:65], v[152:155], v[148:151], v[50:65]
	v_mfma_f32_32x32x16_f16 v[82:97], v[156:159], v[144:147], v[82:97]
	v_mfma_f32_32x32x16_f16 v[18:33], v[156:159], v[148:151], v[18:33]
	ds_read_b128 v[152:155], v130 offset:8192
	ds_read_b128 v[156:159], v130 offset:12288
	s_waitcnt vmcnt(10)
	v_add_u32_e32 v130, v142, v139
	s_waitcnt lgkmcnt(0)
	v_mfma_f32_32x32x16_f16 v[98:113], v[152:155], v[144:147], v[98:113]
	v_mfma_f32_32x32x16_f16 v[34:49], v[152:155], v[148:151], v[34:49]
	v_mfma_f32_32x32x16_f16 v[66:81], v[156:159], v[144:147], v[66:81]
	v_mfma_f32_32x32x16_f16 v[2:17], v[156:159], v[148:151], v[2:17]
	ds_read_b128 v[144:147], v137 offset:4096
	ds_read_b128 v[148:151], v137 offset:5120
	ds_read_b128 v[152:155], v130
	ds_read_b128 v[156:159], v130 offset:4096
	s_waitcnt lgkmcnt(0)
	v_mfma_f32_32x32x16_f16 v[114:129], v[152:155], v[144:147], v[114:129]
	v_mfma_f32_32x32x16_f16 v[50:65], v[152:155], v[148:151], v[50:65]
	v_mfma_f32_32x32x16_f16 v[82:97], v[156:159], v[144:147], v[82:97]
	v_mfma_f32_32x32x16_f16 v[18:33], v[156:159], v[148:151], v[18:33]
	ds_read_b128 v[152:155], v130 offset:8192
	ds_read_b128 v[156:159], v130 offset:12288
	s_waitcnt vmcnt(8)
	v_add_u32_e32 v130, v142, v136
	s_waitcnt lgkmcnt(0)
	v_mfma_f32_32x32x16_f16 v[98:113], v[152:155], v[144:147], v[98:113]
	v_mfma_f32_32x32x16_f16 v[34:49], v[152:155], v[148:151], v[34:49]
	v_mfma_f32_32x32x16_f16 v[66:81], v[156:159], v[144:147], v[66:81]
	v_mfma_f32_32x32x16_f16 v[2:17], v[156:159], v[148:151], v[2:17]
	ds_read_b128 v[144:147], v137 offset:6144
	ds_read_b128 v[148:151], v137 offset:7168
	ds_read_b128 v[152:155], v130
	ds_read_b128 v[156:159], v130 offset:4096
	s_waitcnt lgkmcnt(0)
	v_mfma_f32_32x32x16_f16 v[114:129], v[152:155], v[144:147], v[114:129]
	v_mfma_f32_32x32x16_f16 v[50:65], v[152:155], v[148:151], v[50:65]
	v_mfma_f32_32x32x16_f16 v[82:97], v[156:159], v[144:147], v[82:97]
	v_mfma_f32_32x32x16_f16 v[18:33], v[156:159], v[148:151], v[18:33]
	ds_read_b128 v[152:155], v130 offset:8192
	ds_read_b128 v[156:159], v130 offset:12288
	s_waitcnt lgkmcnt(0)
	s_barrier
	v_or_b32_e32 v130, 0x24000, v138
	s_waitcnt vmcnt(6)
	v_add_u32_e32 v131, v130, v141
	s_waitcnt lgkmcnt(0)
	v_mfma_f32_32x32x16_f16 v[98:113], v[152:155], v[144:147], v[98:113]
	v_mfma_f32_32x32x16_f16 v[34:49], v[152:155], v[148:151], v[34:49]
	v_mfma_f32_32x32x16_f16 v[66:81], v[156:159], v[144:147], v[66:81]
	v_mfma_f32_32x32x16_f16 v[2:17], v[156:159], v[148:151], v[2:17]
	ds_read_b128 v[142:145], v137 offset:8192
	ds_read_b128 v[146:149], v137 offset:9216
	ds_read_b128 v[150:153], v131
	ds_read_b128 v[154:157], v131 offset:4096
	s_waitcnt lgkmcnt(0)
	v_mfma_f32_32x32x16_f16 v[114:129], v[150:153], v[142:145], v[114:129]
	v_mfma_f32_32x32x16_f16 v[50:65], v[150:153], v[146:149], v[50:65]
	v_mfma_f32_32x32x16_f16 v[82:97], v[154:157], v[142:145], v[82:97]
	v_mfma_f32_32x32x16_f16 v[18:33], v[154:157], v[146:149], v[18:33]
	ds_read_b128 v[150:153], v131 offset:8192
	ds_read_b128 v[154:157], v131 offset:12288
	s_waitcnt vmcnt(4)
	v_add_u32_e32 v131, v130, v140
	s_waitcnt lgkmcnt(0)
	v_mfma_f32_32x32x16_f16 v[98:113], v[150:153], v[142:145], v[98:113]
	v_mfma_f32_32x32x16_f16 v[34:49], v[150:153], v[146:149], v[34:49]
	v_mfma_f32_32x32x16_f16 v[66:81], v[154:157], v[142:145], v[66:81]
	v_mfma_f32_32x32x16_f16 v[2:17], v[154:157], v[146:149], v[2:17]
	ds_read_b128 v[142:145], v137 offset:10240
	ds_read_b128 v[146:149], v137 offset:11264
	ds_read_b128 v[150:153], v131
	ds_read_b128 v[154:157], v131 offset:4096
	s_waitcnt lgkmcnt(0)
	v_mfma_f32_32x32x16_f16 v[114:129], v[150:153], v[142:145], v[114:129]
	v_mfma_f32_32x32x16_f16 v[50:65], v[150:153], v[146:149], v[50:65]
	v_mfma_f32_32x32x16_f16 v[82:97], v[154:157], v[142:145], v[82:97]
	v_mfma_f32_32x32x16_f16 v[18:33], v[154:157], v[146:149], v[18:33]
	ds_read_b128 v[150:153], v131 offset:8192
	ds_read_b128 v[154:157], v131 offset:12288
	s_waitcnt vmcnt(2)
	v_add_u32_e32 v131, v130, v139
	v_add_u32_e32 v130, v130, v136
	s_waitcnt lgkmcnt(0)
	v_mfma_f32_32x32x16_f16 v[98:113], v[150:153], v[142:145], v[98:113]
	v_mfma_f32_32x32x16_f16 v[34:49], v[150:153], v[146:149], v[34:49]
	v_mfma_f32_32x32x16_f16 v[66:81], v[154:157], v[142:145], v[66:81]
	v_mfma_f32_32x32x16_f16 v[2:17], v[154:157], v[146:149], v[2:17]
	ds_read_b128 v[140:143], v137 offset:12288
	ds_read_b128 v[144:147], v137 offset:13312
	ds_read_b128 v[148:151], v131
	ds_read_b128 v[152:155], v131 offset:4096
	s_waitcnt lgkmcnt(0)
	v_mfma_f32_32x32x16_f16 v[114:129], v[148:151], v[140:143], v[114:129]
	v_mfma_f32_32x32x16_f16 v[50:65], v[148:151], v[144:147], v[50:65]
	v_mfma_f32_32x32x16_f16 v[82:97], v[152:155], v[140:143], v[82:97]
	v_mfma_f32_32x32x16_f16 v[18:33], v[152:155], v[144:147], v[18:33]
	ds_read_b128 v[148:151], v131 offset:8192
	ds_read_b128 v[152:155], v131 offset:12288
	s_waitcnt vmcnt(0)
	s_waitcnt lgkmcnt(0)
	v_mfma_f32_32x32x16_f16 v[98:113], v[148:151], v[140:143], v[98:113]
	v_mfma_f32_32x32x16_f16 v[34:49], v[148:151], v[144:147], v[34:49]
	v_mfma_f32_32x32x16_f16 v[66:81], v[152:155], v[140:143], v[66:81]
	v_mfma_f32_32x32x16_f16 v[2:17], v[152:155], v[144:147], v[2:17]
	ds_read_b128 v[138:141], v137 offset:14336
	ds_read_b128 v[142:145], v137 offset:15360
	ds_read_b128 v[146:149], v130
	ds_read_b128 v[150:153], v130 offset:4096
	s_waitcnt lgkmcnt(0)
	v_mfma_f32_32x32x16_f16 v[114:129], v[146:149], v[138:141], v[114:129]
	v_mfma_f32_32x32x16_f16 v[50:65], v[146:149], v[142:145], v[50:65]
	s_waitcnt vmcnt(0)
	s_nop 9
	v_fma_f32 v114, 0.5, v114, v134
	v_max_f32_e32 v114, 0, v114
	v_fma_f32 v115, 0.5, v115, v134
	v_add_f32_e32 v114, 0, v114
	v_max_f32_e32 v115, 0, v115
	v_add_f32_e32 v114, v114, v115
	v_fma_f32 v50, 0.5, v50, v133
	v_mfma_f32_32x32x16_f16 v[82:97], v[150:153], v[138:141], v[82:97]
	v_max_f32_e32 v50, 0, v50
	v_fma_f32 v51, 0.5, v51, v133
	v_add_f32_e32 v50, 0, v50
	v_max_f32_e32 v51, 0, v51
	v_add_f32_e32 v50, v50, v51
	s_nop 6
	v_fma_f32 v82, 0.5, v82, v134
	v_mfma_f32_32x32x16_f16 v[18:33], v[150:153], v[142:145], v[18:33]
	ds_read_b128 v[146:149], v130 offset:8192
	ds_read_b128 v[150:153], v130 offset:12288
	v_max_f32_e32 v82, 0, v82
	v_fma_f32 v83, 0.5, v83, v134
	v_max_f32_e32 v83, 0, v83
	s_waitcnt lgkmcnt(0)
	s_barrier
	s_waitcnt lgkmcnt(1)
	v_mfma_f32_32x32x16_f16 v[98:113], v[146:149], v[138:141], v[98:113]
	s_nop 3
	v_fma_f32 v18, 0.5, v18, v133
	v_max_f32_e32 v18, 0, v18
	v_fma_f32 v19, 0.5, v19, v133
	v_max_f32_e32 v19, 0, v19
	v_mfma_f32_32x32x16_f16 v[34:49], v[146:149], v[142:145], v[34:49]
	s_nop 2
	v_fma_f32 v98, 0.5, v98, v134
	v_max_f32_e32 v98, 0, v98
	v_fma_f32 v99, 0.5, v99, v134
	v_add_f32_e32 v98, 0, v98
	v_max_f32_e32 v99, 0, v99
	v_fma_f32 v100, 0.5, v100, v134
	v_add_f32_e32 v98, v98, v99
	s_nop 1
	v_fma_f32 v34, 0.5, v34, v133
	v_max_f32_e32 v34, 0, v34
	v_fma_f32 v35, 0.5, v35, v133
	v_fma_f32 v99, 0.5, v116, v134
	v_max_f32_e32 v100, 0, v100
	v_add_f32_e32 v34, 0, v34
	v_max_f32_e32 v35, 0, v35
	v_fma_f32 v36, 0.5, v36, v133
	v_max_f32_e32 v99, 0, v99
	v_add_f32_e32 v98, v98, v100
	v_fma_f32 v100, 0.5, v117, v134
	v_add_f32_e32 v34, v34, v35
	v_fma_f32 v35, 0.5, v52, v133
	v_max_f32_e32 v36, 0, v36
	v_add_f32_e32 v99, v114, v99
	v_max_f32_e32 v100, 0, v100
	v_max_f32_e32 v35, 0, v35
	v_add_f32_e32 v34, v34, v36
	v_fma_f32 v36, 0.5, v53, v133
	v_add_f32_e32 v99, v99, v100
	v_fma_f32 v100, 0.5, v101, v134
	v_add_f32_e32 v35, v50, v35
	v_max_f32_e32 v36, 0, v36
	v_max_f32_e32 v100, 0, v100
	v_add_f32_e32 v35, v35, v36
	v_fma_f32 v36, 0.5, v37, v133
	v_add_f32_e32 v98, v98, v100
	v_fma_f32 v100, 0.5, v118, v134
	v_max_f32_e32 v36, 0, v36
	v_max_f32_e32 v100, 0, v100
	v_add_f32_e32 v34, v34, v36
	v_fma_f32 v36, 0.5, v54, v133
	v_add_f32_e32 v99, v99, v100
	v_fma_f32 v100, 0.5, v102, v134
	v_max_f32_e32 v36, 0, v36
	v_max_f32_e32 v100, 0, v100
	v_add_f32_e32 v35, v35, v36
	v_fma_f32 v36, 0.5, v38, v133
	v_add_f32_e32 v98, v98, v100
	v_fma_f32 v100, 0.5, v119, v134
	v_max_f32_e32 v36, 0, v36
	v_max_f32_e32 v100, 0, v100
	v_add_f32_e32 v34, v34, v36
	v_fma_f32 v36, 0.5, v55, v133
	v_add_f32_e32 v99, v99, v100
	v_fma_f32 v100, 0.5, v103, v134
	v_max_f32_e32 v36, 0, v36
	v_max_f32_e32 v100, 0, v100
	v_add_f32_e32 v35, v35, v36
	v_fma_f32 v36, 0.5, v39, v133
	v_add_f32_e32 v98, v98, v100
	v_fma_f32 v100, 0.5, v120, v134
	v_max_f32_e32 v36, 0, v36
	v_max_f32_e32 v100, 0, v100
	v_add_f32_e32 v34, v34, v36
	v_fma_f32 v36, 0.5, v56, v133
	v_add_f32_e32 v99, v99, v100
	v_fma_f32 v100, 0.5, v104, v134
	v_max_f32_e32 v36, 0, v36
	v_max_f32_e32 v100, 0, v100
	v_add_f32_e32 v35, v35, v36
	v_fma_f32 v36, 0.5, v40, v133
	v_add_f32_e32 v98, v98, v100
	v_fma_f32 v100, 0.5, v121, v134
	v_max_f32_e32 v36, 0, v36
	v_max_f32_e32 v100, 0, v100
	v_add_f32_e32 v34, v34, v36
	v_fma_f32 v36, 0.5, v57, v133
	v_add_f32_e32 v99, v99, v100
	v_fma_f32 v100, 0.5, v105, v134
	v_max_f32_e32 v36, 0, v36
	v_max_f32_e32 v100, 0, v100
	v_add_f32_e32 v35, v35, v36
	v_fma_f32 v36, 0.5, v41, v133
	v_add_f32_e32 v98, v98, v100
	v_fma_f32 v100, 0.5, v122, v134
	v_max_f32_e32 v36, 0, v36
	v_max_f32_e32 v100, 0, v100
	v_add_f32_e32 v34, v34, v36
	v_fma_f32 v36, 0.5, v58, v133
	v_add_f32_e32 v99, v99, v100
	v_fma_f32 v100, 0.5, v106, v134
	v_max_f32_e32 v36, 0, v36
	v_max_f32_e32 v100, 0, v100
	v_add_f32_e32 v35, v35, v36
	v_fma_f32 v36, 0.5, v42, v133
	v_add_f32_e32 v98, v98, v100
	v_fma_f32 v100, 0.5, v123, v134
	v_max_f32_e32 v36, 0, v36
	v_max_f32_e32 v100, 0, v100
	v_add_f32_e32 v34, v34, v36
	v_fma_f32 v36, 0.5, v59, v133
	v_add_f32_e32 v99, v99, v100
	v_fma_f32 v100, 0.5, v107, v134
	v_max_f32_e32 v36, 0, v36
	v_max_f32_e32 v100, 0, v100
	v_add_f32_e32 v35, v35, v36
	v_fma_f32 v36, 0.5, v43, v133
	v_add_f32_e32 v98, v98, v100
	v_fma_f32 v100, 0.5, v124, v134
	v_max_f32_e32 v36, 0, v36
	v_max_f32_e32 v100, 0, v100
	v_add_f32_e32 v34, v34, v36
	v_fma_f32 v36, 0.5, v60, v133
	v_add_f32_e32 v99, v99, v100
	v_fma_f32 v100, 0.5, v108, v134
	v_max_f32_e32 v36, 0, v36
	v_max_f32_e32 v100, 0, v100
	v_add_f32_e32 v35, v35, v36
	v_fma_f32 v36, 0.5, v44, v133
	v_add_f32_e32 v98, v98, v100
	v_fma_f32 v100, 0.5, v125, v134
	v_max_f32_e32 v36, 0, v36
	v_max_f32_e32 v100, 0, v100
	v_add_f32_e32 v34, v34, v36
	v_fma_f32 v36, 0.5, v61, v133
	v_add_f32_e32 v99, v99, v100
	v_fma_f32 v100, 0.5, v109, v134
	v_max_f32_e32 v36, 0, v36
	v_max_f32_e32 v100, 0, v100
	v_add_f32_e32 v35, v35, v36
	v_fma_f32 v36, 0.5, v45, v133
	v_add_f32_e32 v98, v98, v100
	v_fma_f32 v100, 0.5, v126, v134
	v_max_f32_e32 v36, 0, v36
	v_max_f32_e32 v100, 0, v100
	v_add_f32_e32 v34, v34, v36
	v_fma_f32 v36, 0.5, v62, v133
	v_add_f32_e32 v99, v99, v100
	v_fma_f32 v100, 0.5, v110, v134
	v_max_f32_e32 v36, 0, v36
	v_max_f32_e32 v100, 0, v100
	v_add_f32_e32 v35, v35, v36
	v_fma_f32 v36, 0.5, v46, v133
	v_add_f32_e32 v98, v98, v100
	v_fma_f32 v100, 0.5, v127, v134
	v_max_f32_e32 v36, 0, v36
	v_max_f32_e32 v100, 0, v100
	v_add_f32_e32 v34, v34, v36
	v_fma_f32 v36, 0.5, v63, v133
	v_add_f32_e32 v99, v99, v100
	v_fma_f32 v100, 0.5, v111, v134
	v_max_f32_e32 v36, 0, v36
	s_waitcnt lgkmcnt(0)
	v_mfma_f32_32x32x16_f16 v[66:81], v[150:153], v[138:141], v[66:81]
	v_max_f32_e32 v100, 0, v100
	v_add_f32_e32 v35, v35, v36
	v_fma_f32 v36, 0.5, v47, v133
	v_add_f32_e32 v98, v98, v100
	v_fma_f32 v100, 0.5, v128, v134
	v_max_f32_e32 v36, 0, v36
	v_max_f32_e32 v100, 0, v100
	v_mfma_f32_32x32x16_f16 v[2:17], v[150:153], v[142:145], v[2:17]
	v_add_f32_e32 v34, v34, v36
	v_fma_f32 v36, 0.5, v64, v133
	v_add_f32_e32 v99, v99, v100
	v_fma_f32 v100, 0.5, v112, v134
	v_max_f32_e32 v36, 0, v36
	v_max_f32_e32 v100, 0, v100
	v_add_f32_e32 v35, v35, v36
	v_fma_f32 v36, 0.5, v48, v133
	v_add_f32_e32 v98, v98, v100
	v_fma_f32 v100, 0.5, v129, v134
	v_max_f32_e32 v36, 0, v36
	v_max_f32_e32 v100, 0, v100
	v_add_f32_e32 v34, v34, v36
	v_fma_f32 v36, 0.5, v65, v133
	v_add_f32_e32 v99, v99, v100
	v_fma_f32 v100, 0.5, v113, v134
	v_max_f32_e32 v36, 0, v36
	v_max_f32_e32 v100, 0, v100
	v_fma_f32 v66, 0.5, v66, v134
	v_add_f32_e32 v35, v35, v36
	v_fma_f32 v36, 0.5, v49, v133
	v_add_f32_e32 v98, v98, v100
	v_max_f32_e32 v66, 0, v66
	v_fma_f32 v67, 0.5, v67, v134
	v_max_f32_e32 v36, 0, v36
	v_fma_f32 v2, 0.5, v2, v133
	v_add_f32_e32 v66, v98, v66
	v_max_f32_e32 v67, 0, v67
	v_fma_f32 v68, 0.5, v68, v134
	v_add_f32_e32 v34, v34, v36
	v_max_f32_e32 v2, 0, v2
	v_fma_f32 v3, 0.5, v3, v133
	v_add_f32_e32 v82, v99, v82
	v_add_f32_e32 v66, v66, v67
	v_fma_f32 v67, 0.5, v84, v134
	v_max_f32_e32 v68, 0, v68
	v_add_f32_e32 v2, v34, v2
	v_max_f32_e32 v3, 0, v3
	v_fma_f32 v4, 0.5, v4, v133
	v_add_f32_e32 v82, v82, v83
	v_max_f32_e32 v67, 0, v67
	v_add_f32_e32 v66, v66, v68
	v_fma_f32 v68, 0.5, v85, v134
	v_add_f32_e32 v18, v35, v18
	v_add_f32_e32 v2, v2, v3
	v_fma_f32 v3, 0.5, v20, v133
	v_max_f32_e32 v4, 0, v4
	v_add_f32_e32 v67, v82, v67
	v_max_f32_e32 v68, 0, v68
	v_add_f32_e32 v18, v18, v19
	v_max_f32_e32 v3, 0, v3
	v_add_f32_e32 v2, v2, v4
	v_fma_f32 v4, 0.5, v21, v133
	v_add_f32_e32 v67, v67, v68
	v_fma_f32 v68, 0.5, v69, v134
	v_add_f32_e32 v3, v18, v3
	v_max_f32_e32 v4, 0, v4
	v_max_f32_e32 v68, 0, v68
	v_add_f32_e32 v3, v3, v4
	v_fma_f32 v4, 0.5, v5, v133
	v_add_f32_e32 v66, v66, v68
	v_fma_f32 v68, 0.5, v86, v134
	v_max_f32_e32 v4, 0, v4
	v_max_f32_e32 v68, 0, v68
	v_add_f32_e32 v2, v2, v4
	v_fma_f32 v4, 0.5, v22, v133
	v_add_f32_e32 v67, v67, v68
	v_fma_f32 v68, 0.5, v70, v134
	v_max_f32_e32 v4, 0, v4
	v_max_f32_e32 v68, 0, v68
	v_add_f32_e32 v3, v3, v4
	v_fma_f32 v4, 0.5, v6, v133
	v_add_f32_e32 v66, v66, v68
	v_fma_f32 v68, 0.5, v87, v134
	v_max_f32_e32 v4, 0, v4
	v_max_f32_e32 v68, 0, v68
	v_add_f32_e32 v2, v2, v4
	v_fma_f32 v4, 0.5, v23, v133
	v_add_f32_e32 v67, v67, v68
	v_fma_f32 v68, 0.5, v71, v134
	v_max_f32_e32 v4, 0, v4
	v_max_f32_e32 v68, 0, v68
	v_add_f32_e32 v3, v3, v4
	v_fma_f32 v4, 0.5, v7, v133
	v_add_f32_e32 v66, v66, v68
	v_fma_f32 v68, 0.5, v88, v134
	v_max_f32_e32 v4, 0, v4
	v_max_f32_e32 v68, 0, v68
	v_add_f32_e32 v2, v2, v4
	v_fma_f32 v4, 0.5, v24, v133
	v_add_f32_e32 v67, v67, v68
	v_fma_f32 v68, 0.5, v72, v134
	v_max_f32_e32 v4, 0, v4
	v_max_f32_e32 v68, 0, v68
	v_add_f32_e32 v3, v3, v4
	v_fma_f32 v4, 0.5, v8, v133
	v_add_f32_e32 v66, v66, v68
	v_fma_f32 v68, 0.5, v89, v134
	v_max_f32_e32 v4, 0, v4
	v_max_f32_e32 v68, 0, v68
	v_add_f32_e32 v2, v2, v4
	v_fma_f32 v4, 0.5, v25, v133
	v_add_f32_e32 v67, v67, v68
	v_fma_f32 v68, 0.5, v73, v134
	v_max_f32_e32 v4, 0, v4
	v_max_f32_e32 v68, 0, v68
	v_add_f32_e32 v3, v3, v4
	v_fma_f32 v4, 0.5, v9, v133
	v_add_f32_e32 v66, v66, v68
	v_fma_f32 v68, 0.5, v90, v134
	v_max_f32_e32 v4, 0, v4
	v_max_f32_e32 v68, 0, v68
	v_add_f32_e32 v2, v2, v4
	v_fma_f32 v4, 0.5, v26, v133
	v_add_f32_e32 v67, v67, v68
	v_fma_f32 v68, 0.5, v74, v134
	v_max_f32_e32 v4, 0, v4
	v_max_f32_e32 v68, 0, v68
	v_add_f32_e32 v3, v3, v4
	v_fma_f32 v4, 0.5, v10, v133
	v_add_f32_e32 v66, v66, v68
	v_fma_f32 v68, 0.5, v91, v134
	v_max_f32_e32 v4, 0, v4
	v_max_f32_e32 v68, 0, v68
	v_add_f32_e32 v2, v2, v4
	v_fma_f32 v4, 0.5, v27, v133
	v_add_f32_e32 v67, v67, v68
	v_fma_f32 v68, 0.5, v75, v134
	v_max_f32_e32 v4, 0, v4
	v_max_f32_e32 v68, 0, v68
	v_add_f32_e32 v3, v3, v4
	v_fma_f32 v4, 0.5, v11, v133
	v_add_f32_e32 v66, v66, v68
	v_fma_f32 v68, 0.5, v92, v134
	v_max_f32_e32 v4, 0, v4
	v_max_f32_e32 v68, 0, v68
	v_add_f32_e32 v2, v2, v4
	v_fma_f32 v4, 0.5, v28, v133
	v_add_f32_e32 v67, v67, v68
	v_fma_f32 v68, 0.5, v76, v134
	v_max_f32_e32 v4, 0, v4
	v_max_f32_e32 v68, 0, v68
	v_add_f32_e32 v3, v3, v4
	v_fma_f32 v4, 0.5, v12, v133
	v_add_f32_e32 v66, v66, v68
	v_fma_f32 v68, 0.5, v93, v134
	v_max_f32_e32 v4, 0, v4
	v_max_f32_e32 v68, 0, v68
	v_add_f32_e32 v2, v2, v4
	v_fma_f32 v4, 0.5, v29, v133
	v_add_f32_e32 v67, v67, v68
	v_fma_f32 v68, 0.5, v77, v134
	v_max_f32_e32 v4, 0, v4
	v_max_f32_e32 v68, 0, v68
	v_add_f32_e32 v3, v3, v4
	v_fma_f32 v4, 0.5, v13, v133
	v_add_f32_e32 v66, v66, v68
	v_fma_f32 v68, 0.5, v94, v134
	v_max_f32_e32 v4, 0, v4
	v_max_f32_e32 v68, 0, v68
	v_add_f32_e32 v2, v2, v4
	v_fma_f32 v4, 0.5, v30, v133
	v_add_f32_e32 v67, v67, v68
	v_fma_f32 v68, 0.5, v78, v134
	v_max_f32_e32 v4, 0, v4
	v_max_f32_e32 v68, 0, v68
	v_add_f32_e32 v3, v3, v4
	v_fma_f32 v4, 0.5, v14, v133
	v_add_f32_e32 v66, v66, v68
	v_fma_f32 v68, 0.5, v95, v134
	v_max_f32_e32 v4, 0, v4
	v_max_f32_e32 v68, 0, v68
	v_add_f32_e32 v2, v2, v4
	v_fma_f32 v4, 0.5, v31, v133
	v_add_f32_e32 v67, v67, v68
	v_fma_f32 v68, 0.5, v79, v134
	v_max_f32_e32 v4, 0, v4
	v_max_f32_e32 v68, 0, v68
	v_add_f32_e32 v3, v3, v4
	v_fma_f32 v4, 0.5, v15, v133
	v_add_f32_e32 v66, v66, v68
	v_fma_f32 v68, 0.5, v96, v134
	v_max_f32_e32 v4, 0, v4
	v_max_f32_e32 v68, 0, v68
	v_add_f32_e32 v2, v2, v4
	v_fma_f32 v4, 0.5, v32, v133
	v_add_f32_e32 v67, v67, v68
	v_fma_f32 v68, 0.5, v80, v134
	v_max_f32_e32 v4, 0, v4
	v_max_f32_e32 v68, 0, v68
	v_add_f32_e32 v3, v3, v4
	v_fma_f32 v4, 0.5, v16, v133
	v_add_f32_e32 v66, v66, v68
	v_fma_f32 v68, 0.5, v97, v134
	v_max_f32_e32 v4, 0, v4
	v_max_f32_e32 v68, 0, v68
	v_fmac_f32_e32 v134, 0.5, v81
	v_add_f32_e32 v2, v2, v4
	v_fma_f32 v4, 0.5, v33, v133
	v_add_f32_e32 v67, v67, v68
	v_max_f32_e32 v68, 0, v134
	v_max_f32_e32 v4, 0, v4
	v_fmac_f32_e32 v133, 0.5, v17
	v_add_f32_e32 v66, v66, v68
	v_add_f32_e32 v3, v3, v4
	v_max_f32_e32 v4, 0, v133
	v_fma_f32 v66, v135, v66, 0
	v_add_f32_e32 v2, v2, v4
	v_fmac_f32_e32 v66, v132, v2
	v_fma_f32 v67, v135, v67, 0
	v_fmac_f32_e32 v67, v132, v3
	s_nop 1
	v_add_f32_dpp v66, v66, v66 quad_perm:[1,0,3,2] row_mask:0xf bank_mask:0xf
	v_add_f32_dpp v67, v67, v67 quad_perm:[1,0,3,2] row_mask:0xf bank_mask:0xf
	s_nop 0
	v_add_f32_dpp v66, v66, v66 quad_perm:[2,3,0,1] row_mask:0xf bank_mask:0xf
	v_add_f32_dpp v67, v67, v67 quad_perm:[2,3,0,1] row_mask:0xf bank_mask:0xf
	s_nop 0
	v_add_f32_dpp v66, v66, v66 row_half_mirror row_mask:0xf bank_mask:0xf
	v_add_f32_dpp v67, v67, v67 row_half_mirror row_mask:0xf bank_mask:0xf
	s_nop 0
	v_add_f32_dpp v66, v66, v66 row_mirror row_mask:0xf bank_mask:0xf
	v_add_f32_dpp v67, v67, v67 row_mirror row_mask:0xf bank_mask:0xf
	s_nop 0
	v_readlane_b32 s30, v67, 0
	v_readlane_b32 s31, v67, 16
	v_readlane_b32 s32, v67, 32
	v_readlane_b32 s33, v67, 48
	v_readlane_b32 s34, v66, 0
	v_readlane_b32 s35, v66, 16
	v_readlane_b32 s36, v66, 32
	v_readlane_b32 s37, v66, 48
	v_mov_b32_e32 v2, s30
	v_mov_b32_e32 v3, s34
	v_add_f32_e32 v2, s31, v2
	v_add_f32_e32 v3, s35, v3
	v_add_f32_e32 v2, s32, v2
	v_add_f32_e32 v3, s36, v3
	v_add_f32_e32 v2, s33, v2
	v_add_f32_e32 v3, s37, v3
	v_cmp_eq_u32_e32 vcc, 0, v1
	s_and_saveexec_b64 s[6:7], vcc
	s_cbranch_execz .LBB1_9
	s_or_b32 s4, s12, 1
	s_lshl_b64 s[8:9], s[4:5], 5
	s_add_u32 s8, s10, s8
	s_mov_b32 s13, s5
	s_addc_u32 s9, s11, s9
	s_lshl_b32 s3, s14, 2
	s_lshl_b64 s[4:5], s[12:13], 5
	s_add_u32 s4, s10, s4
	s_addc_u32 s5, s11, s5
	v_mov_b32_e32 v4, s3
	global_store_dword v4, v2, s[4:5]
	global_store_dword v4, v3, s[8:9]
